# stream: one wave per block re-touches the last launch's code and kernarg lines just before ending; prep as v35
# baseline (speedup 1.0000x reference)
_Z13stream_kernelPKfPf:
	s_mov_b64 s[12:13], s[0:1]
	s_load_dwordx4 s[4:7], s[0:1], 0x0
	s_movk_i32 s0, 0x100
	v_readfirstlane_b32 s3, v0
	v_cmp_gt_u32_e32 vcc, s0, v0
	s_and_saveexec_b64 s[0:1], vcc
	s_cbranch_execz .LBB1_2
	v_lshlrev_b32_e32 v18, 4, v0
	v_mov_b32_e32 v19, 0
	s_waitcnt lgkmcnt(0)
	v_lshl_add_u64 v[14:15], s[6:7], 0, v[18:19]
	v_add_co_u32_e32 v16, vcc, 0x1000, v14
	global_load_dwordx4 v[2:5], v18, s[6:7]
	s_nop 0
	v_addc_co_u32_e32 v17, vcc, 0, v15, vcc
	v_add_co_u32_e32 v20, vcc, 0x2000, v14
	s_nop 1
	v_addc_co_u32_e32 v21, vcc, 0, v15, vcc
	v_add_co_u32_e32 v14, vcc, 0x3000, v14
	global_load_dwordx4 v[6:9], v[16:17], off
	global_load_dwordx4 v[10:13], v[20:21], off
	v_addc_co_u32_e32 v15, vcc, 0, v15, vcc
	global_load_dwordx4 v[14:17], v[14:15], off
	s_waitcnt vmcnt(2)
	v_pk_add_f32 v[4:5], v[4:5], v[8:9]
	v_pk_add_f32 v[2:3], v[2:3], v[6:7]
	s_waitcnt vmcnt(1)
	v_pk_add_f32 v[4:5], v[4:5], v[12:13]
	v_pk_add_f32 v[2:3], v[2:3], v[10:11]
	s_waitcnt vmcnt(0)
	v_pk_add_f32 v[4:5], v[4:5], v[16:17]
	v_pk_add_f32 v[2:3], v[2:3], v[14:15]
	ds_write_b128 v18, v[2:5]

.LBB1_4:
	s_mov_b64 exec, -1
	s_cmp_lg_u32 s8, 0
	s_cbranch_scc1 .Lst_end
	s_getpc_b64 s[10:11]
	s_and_b32 s10, s10, 0xffffff00
	v_lshlrev_b32_e32 v60, 4, v24
	global_load_dwordx4 v[62:65], v60, s[10:11]
	global_load_dwordx4 v[62:65], v60, s[10:11] offset:1024
	global_load_dwordx4 v[62:65], v60, s[10:11] offset:2048
	s_and_b32 s10, s12, 0xffffffc0
	s_mov_b32 s11, s13
	v_add_u32_e32 v61, s10, v60
	v_xor_b32_e32 v61, s12, v61
	v_cmp_gt_u32_e32 vcc, 0x1000, v61
	s_and_b64 exec, exec, vcc
	s_cbranch_execz .Lst_end
	global_load_dwordx4 v[62:65], v60, s[10:11]

	.amdhsa_kernel _Z13stream_kernelPKfPf
		.amdhsa_group_segment_fixed_size 4096
		.amdhsa_private_segment_fixed_size 0
		.amdhsa_kernarg_size 16
		.amdhsa_user_sgpr_count 2
		.amdhsa_user_sgpr_dispatch_ptr 0
		.amdhsa_user_sgpr_queue_ptr 0
		.amdhsa_user_sgpr_kernarg_segment_ptr 1
		.amdhsa_user_sgpr_dispatch_id 0
		.amdhsa_user_sgpr_kernarg_preload_length 0
		.amdhsa_user_sgpr_kernarg_preload_offset 0
		.amdhsa_user_sgpr_private_segment_size 0
		.amdhsa_uses_dynamic_stack 0
		.amdhsa_enable_private_segment 0
		.amdhsa_system_sgpr_workgroup_id_x 1
		.amdhsa_system_sgpr_workgroup_id_y 0
		.amdhsa_system_sgpr_workgroup_id_z 0
		.amdhsa_system_sgpr_workgroup_info 0
		.amdhsa_system_vgpr_workitem_id 0
		.amdhsa_next_free_vgpr 67
		.amdhsa_next_free_sgpr 14
		.amdhsa_accum_offset 68
		.amdhsa_reserve_vcc 1
		.amdhsa_float_round_mode_32 0
		.amdhsa_float_round_mode_16_64 0
		.amdhsa_float_denorm_mode_32 3
		.amdhsa_float_denorm_mode_16_64 3
		.amdhsa_dx10_clamp 1
		.amdhsa_ieee_mode 1
		.amdhsa_fp16_overflow 0
		.amdhsa_tg_split 0
		.amdhsa_exception_fp_ieee_invalid_op 0
		.amdhsa_exception_fp_denorm_src 0
		.amdhsa_exception_fp_ieee_div_zero 0
		.amdhsa_exception_fp_ieee_overflow 0
		.amdhsa_exception_fp_ieee_underflow 0
		.amdhsa_exception_fp_ieee_inexact 0
		.amdhsa_exception_int_div_zero 0
	.end_amdhsa_kernel

.Lfunc_end1:
	.size	_Z13stream_kernelPKfPf, .Lfunc_end1-_Z13stream_kernelPKfPf
	.set _Z13stream_kernelPKfPf.num_vgpr, 67
	.set _Z13stream_kernelPKfPf.num_agpr, 0
	.set _Z13stream_kernelPKfPf.numbered_sgpr, 14
	.set _Z13stream_kernelPKfPf.num_named_barrier, 0
	.set _Z13stream_kernelPKfPf.private_seg_size, 0
	.set _Z13stream_kernelPKfPf.uses_vcc, 1
	.set _Z13stream_kernelPKfPf.uses_flat_scratch, 0
	.set _Z13stream_kernelPKfPf.has_dyn_sized_stack, 0
	.set _Z13stream_kernelPKfPf.has_recursion, 0
	.set _Z13stream_kernelPKfPf.has_indirect_call, 0

amdhsa.kernels:
  - .agpr_count:     0
    .args:
      - .actual_access:  read_only
        .address_space:  global
        .offset:         0
        .size:           8
        .value_kind:     global_buffer
      - .actual_access:  read_only
        .address_space:  global
        .offset:         8
        .size:           8
        .value_kind:     global_buffer
      - .actual_access:  read_only
        .address_space:  global
        .offset:         16
        .size:           8
        .value_kind:     global_buffer
      - .actual_access:  read_only
        .address_space:  global
        .offset:         24
        .size:           8
        .value_kind:     global_buffer
      - .actual_access:  write_only
        .address_space:  global
        .offset:         32
        .size:           8
        .value_kind:     global_buffer
    .group_segment_fixed_size: 2112
    .kernarg_segment_align: 8
    .kernarg_segment_size: 40
    .language:       OpenCL C
    .language_version:
      - 2
      - 0
    .max_flat_workgroup_size: 1024
    .name:           _Z11prep_kernelPKfS0_S0_S0_Pf
    .private_segment_fixed_size: 0
    .sgpr_count:     34
    .sgpr_spill_count: 0
    .symbol:         _Z11prep_kernelPKfS0_S0_S0_Pf.kd
    .uniform_work_group_size: 1
    .uses_dynamic_stack: false
    .vgpr_count:     72
    .vgpr_spill_count: 0
    .wavefront_size: 64
  - .agpr_count:     0
    .args:
      - .actual_access:  read_only
        .address_space:  global
        .offset:         0
        .size:           8
        .value_kind:     global_buffer
      - .address_space:  global
        .offset:         8
        .size:           8
        .value_kind:     global_buffer
    .group_segment_fixed_size: 4096
    .kernarg_segment_align: 8
    .kernarg_segment_size: 16
    .language:       OpenCL C
    .language_version:
      - 2
      - 0
    .max_flat_workgroup_size: 1024
    .name:           _Z13stream_kernelPKfPf
    .private_segment_fixed_size: 0
    .sgpr_count:     20
    .sgpr_spill_count: 0
    .symbol:         _Z13stream_kernelPKfPf.kd
    .uniform_work_group_size: 1
    .uses_dynamic_stack: false
    .vgpr_count:     67
    .vgpr_spill_count: 0
    .wavefront_size: 64
  - .agpr_count:     0
    .args:
      - .actual_access:  read_only
        .address_space:  global
        .offset:         0
        .size:           8
        .value_kind:     global_buffer
      - .actual_access:  write_only
        .address_space:  global
        .offset:         8
        .size:           8
        .value_kind:     global_buffer
    .group_segment_fixed_size: 32
    .kernarg_segment_align: 8
    .kernarg_segment_size: 16
    .language:       OpenCL C
    .language_version:
      - 2
      - 0
    .max_flat_workgroup_size: 256
    .name:           _Z14softmax_kernelPKfPf
    .private_segment_fixed_size: 0
    .sgpr_count:     16
    .sgpr_spill_count: 0
    .symbol:         _Z14softmax_kernelPKfPf.kd
    .uniform_work_group_size: 1
    .uses_dynamic_stack: false
    .vgpr_count:     17
    .vgpr_spill_count: 0
    .wavefront_size: 64
